# up-projection phase: GEMM units re-dealt so the long K=1024 in-proj tail tile runs on the 64 workgroups with the lightest block-choice work and no kv/q units
# speedup vs baseline: 1.0020x; 1.0020x over previous
;     __device__ bool next(int i, Unit& u) const { const bool ok = StaticOrder::next(i, u); u.pn += pn0; return ok; }
;     __device__ bool next(int i, Unit& u) const {
;         const long L = (long)i * G + c; if (L >= nwg) return false;
;         int wgid = (int)L; { const int q = nwg / NXCD, r = nwg % NXCD, xcd = wgid % NXCD, off = wgid / NXCD; wgid = (xcd < r ? xcd * (q + 1) : r * (q + 1) + (xcd - r) * q) + off; }
;         const int nig = WGM * nN, gid = wgid / nig, fm = gid * WGM, gsz = (nM - fm) < WGM ? (nM - fm) : WGM;
;         u.pm = fm + ((wgid % nig) % gsz); u.pn = (wgid % nig) / gsz; u.e = 0; u.r0 = u.pm * BM; u.rend = u.r0 + BM; return true;
; __global__ void __launch_bounds__(NTHR, 2) mk(Params p) {
;     ...
;             { const int G3 = F.G - F.G / 4;
;               pg8::Gemm g{CKVN, WukvT + (size_t)l * SZ_WUKV, T, 1024, KVL, KVL, KVL}; pg8::StaticOrder S; S.init(T, 1024, G3, (int)blockIdx.x < G3 ? (int)blockIdx.x : (1 << 28));
;               EpiKV E{KB, VB}; pg8::gemm_phase<EpiKV, pg8::StaticOrder, true>(F.lds, g, S, E); }
.LBB0_428:
	s_or_b64 exec, exec, s[2:3]
	s_lshr_b32 s0, s38, 30
	s_add_i32 s0, s59, s0
	s_ashr_i32 s0, s0, 2
	s_sub_i32 s33, s59, s0
	v_readlane_b32 s0, v253, 2
	s_add_i32 s39, s0, -64
	s_cmpk_lt_i32 s0, 0xc0
	s_cselect_b32 s39, 0x10000000, s39
	s_cmpk_lt_i32 s0, 0x80
	s_cselect_b32 s39, s0, s39
	v_readlane_b32 s1, v253, 3
	v_mov_b32_e32 v2, v0
	s_cmpk_lt_i32 s39, 0x100
	s_barrier
	s_cselect_b64 s[0:1], -1, 0
	s_cmpk_gt_i32 s39, 0xff
	v_readfirstlane_b32 s4, v2
	s_cbranch_scc1 .LBB0_434
	s_ashr_i32 s2, s39, 31
	s_lshr_b32 s2, s2, 29
	s_add_i32 s7, s39, s2
	s_and_b32 s2, s7, -8
	s_sub_i32 s5, s39, s2
	s_cmp_gt_i32 s5, -1
	s_cbranch_scc0 .LBB0_431
	s_lshl_b32 s6, s5, 5
	s_ashr_i32 s2, s7, 3
	s_cbranch_execz .LBB0_432
	s_branch .LBB0_433

;     __device__ bool next(int i, Unit& u) const { const bool ok = StaticOrder::next(i, u); u.pn += pn0; return ok; }
;     __device__ bool next(int i, Unit& u) const {
;         const long L = (long)i * G + c; if (L >= nwg) return false;
;         int wgid = (int)L; { const int q = nwg / NXCD, r = nwg % NXCD, xcd = wgid % NXCD, off = wgid / NXCD; wgid = (xcd < r ? xcd * (q + 1) : r * (q + 1) + (xcd - r) * q) + off; }
;         const int nig = WGM * nN, gid = wgid / nig, fm = gid * WGM, gsz = (nM - fm) < WGM ? (nM - fm) : WGM;
;         u.pm = fm + ((wgid % nig) % gsz); u.pn = (wgid % nig) / gsz; u.e = 0; u.r0 = u.pm * BM; u.rend = u.r0 + BM; return true;
; __global__ void __launch_bounds__(NTHR, 2) mk(Params p) {
;     ...
;             { pg8::Gemm g{CQN, WuqT + (size_t)l * SZ_WUQ, T, 768, QL, QL, QL}; pg8::StaticOrder S; S.init(T, 768, F.G, (int)blockIdx.x);
;               EpiQ E{QB, CS}; pg8::gemm_phase<EpiQ, pg8::StaticOrder, true>(F.lds, g, S, E); }
.LBB0_527:
	v_readlane_b32 s0, v253, 2
	s_bitcmp0_b32 s0, 7
	s_cbranch_scc1 .Lq19_0_0
	s_xor_b32 s0, s0, 64
.Lq19_0_0:
	v_mov_b32_e32 v2, v0
	v_readlane_b32 s1, v253, 3
	s_mov_b32 s2, s0
	s_cmpk_lt_i32 s0, 0xc0
	s_cselect_b64 s[0:1], -1, 0
	s_cmpk_gt_i32 s2, 0xbf
	v_readfirstlane_b32 s4, v2
	s_cbranch_scc1 .LBB0_529
	v_readlane_b32 s2, v253, 2
	s_bitcmp0_b32 s2, 7
	s_cbranch_scc1 .Lq19_0_1
	s_xor_b32 s2, s2, 64
.Lq19_0_1:
	s_mov_b32 s6, s2
	s_ashr_i32 s2, s2, 31
	s_lshr_b32 s2, s2, 29
	v_readlane_b32 s3, v253, 3
	s_add_i32 s2, s6, s2
	s_ashr_i32 s3, s2, 3
	s_and_b32 s2, s2, -8
	s_sub_i32 s2, s6, s2
	s_cmp_lt_i32 s2, 0
	s_cselect_b32 s5, 25, 24
	s_mul_i32 s2, s2, s5
	s_add_i32 s2, s2, s3
	s_mul_hi_i32 s3, s2, 0x2aaaaaab
	s_lshr_b32 s5, s3, 31
	s_ashr_i32 s3, s3, 2
	s_add_i32 s3, s3, s5
	s_lshl_b32 s5, s3, 3
	s_mul_i32 s3, s3, 24
	s_sub_i32 s2, s2, s3
	s_bfe_i32 s3, s2, 0x80000
	s_bfe_u32 s3, s3, 0x3000c
	s_add_i32 s3, s2, s3
	s_bfe_i32 s6, s3, 0x80000
	s_and_b32 s3, s3, 0xf8
	s_sub_i32 s2, s2, s3
	s_sext_i32_i8 s2, s2
	s_add_i32 s53, s5, s2
	s_sext_i32_i16 s6, s6
	s_lshl_b32 s18, s53, 8
	s_ashr_i32 s52, s6, 3
	s_add_i32 s19, s18, 0x100

;     __device__ __forceinline__ const char* b_ptr(const Gemm& g, const Unit& u) const { return (const char*)g.Bt + (size_t)u.pn * BM * g.ldb * 2; }
;     __device__ bool next(int i, Unit& u) const { const bool ok = StaticOrder::next(i, u); u.pn += pn0; return ok; }
; #define PG8_STAGE_B(bufoff, gbase) do { _Pragma("unroll") for (int _i = 0; _i < 2; ++_i) \
;         __builtin_amdgcn_global_load_lds((const unsigned*)((const char*)(gbase) + voffB[_i]), (LAS unsigned*)(lds + (bufoff) + ldsw + _i * 8192), 16, 0, 0); } while (0)
; #define PG8_STAGE_A(bufoff, V0, V1, kb) do { \
;         __builtin_amdgcn_global_load_lds((const unsigned*)((Abase + (kb)) + (V0)), (LAS unsigned*)(lds + (bufoff) + ldsw), 16, 0, 0); \
;         __builtin_amdgcn_global_load_lds((const unsigned*)((Abase + (kb)) + (V1)), (LAS unsigned*)(lds + (bufoff) + ldsw + 8192), 16, 0, 0); } while (0)
; #define PG8_WAIT_V(n) asm volatile("s_waitcnt vmcnt(" #n ")" ::: "memory")
; #define PG8_BAR __builtin_amdgcn_s_barrier()
;     __device__ __forceinline__ const char* b_ptr(const pg8::Gemm& g, const pg8::Unit& u) const { return (const char*)g.Bt + (size_t)u.e * strideE + (size_t)u.pn * 256 * g.ldb * 2; }
; template <class Epi, class Sched, bool ALIGN_EPI>
; __device__ __forceinline__ void gemm_phase(LAS unsigned char* lds, const Gemm g, const Sched& S, const Epi& E) {
;     ...
;     PG8_STAGE_B(PG8_SB(0, 0), cB); PG8_STAGE_B(PG8_SB(0, 1), cB + hstepB); PG8_STAGE_A(PG8_SA(0, 0), vc00, vc01, 0u); PG8_STAGE_A(PG8_SA(0, 1), vc10, vc11, 0u);
;     PG8_STAGE_B(PG8_SB(1, 0), cB + 128); PG8_STAGE_A(PG8_SA(1, 0), vc00, vc01, 128u); PG8_STAGE_B(PG8_SB(1, 1), cB + hstepB + 128);
;     if (wr == 1) PG8_BAR;
;     PG8_WAIT_V(8); PG8_BAR;
;     PG8_WAIT_V(6); PG8_BAR;
;     }
;     for (;;) {
;         const bool has_next = S.next(ui + 1, nxt);
;         const char* nB = cB; const float* pbn = pbc;
;         if constexpr (Sched::BF32) { if (has_next) pbn = S.bsrc(nxt, bh); } else { if (has_next) nB = S.b_ptr(g, nxt); }
;         unsigned vn00 = vc00, vn01 = vc01, vn10 = vc10, vn11 = vc11;
;         if (has_next) { PG8_VOFF(vn, nxt); }
.LBB0_532:
	v_lshrrev_b32_e32 v5, 1, v2
	v_and_b32_e32 v5, 24, v5
	v_and_b32_e32 v4, 15, v2
	v_lshlrev_b32_e32 v6, 1, v5
	v_lshlrev_b32_e32 v2, 2, v2
	v_lshl_or_b32 v203, s0, 6, v4
	s_lshl_b32 s0, s0, 13
	v_lshl_or_b32 v4, v4, 6, v6
	v_and_b32_e32 v2, 32, v2
	v_bitop3_b32 v6, v4, s0, v2 bitop3:0xde
	s_lshl_b32 s0, s1, 5
	s_and_b32 s0, s0, 0x60
	s_lshl_b32 s1, s0, 7
	s_waitcnt vmcnt(8)
	s_barrier
	s_waitcnt vmcnt(6)
	s_cmpk_lt_u32 s4, 0x100
	v_readlane_b32 s4, v253, 2
	s_movk_i32 s37, 0x60
	v_bitop3_b32 v221, v4, s1, v2 bitop3:0xde
	s_cselect_b64 s[12:13], -1, 0
	s_bitcmp0_b32 s4, 7
	s_cbranch_scc1 .Lq19_0_2
	s_xor_b32 s4, s4, 64
.Lq19_0_2:
	s_ashr_i32 s39, s4, 31
	v_or_b32_e32 v223, s0, v5
	v_mov_b64_e32 v[206:207], 0xc0
	v_mov_b64_e32 v[208:209], 0xbf
	s_mov_b32 s40, 0x2aaaaaab
	s_add_i32 s41, 0, 0x10000
	s_add_i32 s44, 0, 0x14000
	s_add_i32 s45, 0, 0x18000
	s_add_i32 s46, 0, 0x1c000
	s_mov_b32 s14, 0x3e16c740
	s_movk_i32 s47, 0x600
	v_add_u32_e32 v234, 0, v6
	s_barrier
	v_readlane_b32 s5, v253, 3
	s_branch .LBB0_535

;     __device__ bool next(int i, Unit& u) const { const bool ok = StaticOrder::next(i, u); u.pn += pn0; return ok; }
;     __device__ bool next(int i, Unit& u) const {
;         const long L = (long)i * G + c; if (L >= nwg) return false;
;         int wgid = (int)L; { const int q = nwg / NXCD, r = nwg % NXCD, xcd = wgid % NXCD, off = wgid / NXCD; wgid = (xcd < r ? xcd * (q + 1) : r * (q + 1) + (xcd - r) * q) + off; }
;         const int nig = WGM * nN, gid = wgid / nig, fm = gid * WGM, gsz = (nM - fm) < WGM ? (nM - fm) : WGM;
;         u.pm = fm + ((wgid % nig) % gsz); u.pn = (wgid % nig) / gsz; u.e = 0; u.r0 = u.pm * BM; u.rend = u.r0 + BM; return true;
; template <class Epi, class Sched, bool ALIGN_EPI>
; __device__ __forceinline__ void gemm_phase(LAS unsigned char* lds, const Gemm g, const Sched& S, const Epi& E) {
;     ...
;         const bool has_next = S.next(ui + 1, nxt);
.LBB0_535:
	s_add_i32 s36, s36, 1
	s_mul_i32 s0, s36, s38
	s_mul_hi_u32 s1, s36, s59
	s_add_i32 s1, s1, s0
	s_mul_i32 s0, s36, s59
	v_readlane_b32 s4, v253, 2
	s_bitcmp0_b32 s4, 7
	s_cbranch_scc1 .Lq19_0_3
	s_xor_b32 s4, s4, 64
.Lq19_0_3:
	s_add_u32 s0, s0, s4
	s_addc_u32 s1, s1, s39
	v_readlane_b32 s5, v253, 3
	v_cmp_gt_i64_e32 vcc, s[0:1], v[208:209]
	v_cmp_lt_i64_e64 s[4:5], s[0:1], v[206:207]
	s_cbranch_vccnz .LBB0_537
	s_ashr_i32 s1, s0, 31
	s_lshr_b32 s1, s1, 29
	s_add_i32 s1, s0, s1
	s_ashr_i32 s16, s1, 3
	s_and_b32 s1, s1, -8
	s_sub_i32 s0, s0, s1
	s_cmp_lt_i32 s0, 0
	s_cselect_b32 s1, 25, 24
	s_mul_i32 s0, s0, s1
	s_add_i32 s0, s0, s16
	s_mul_hi_i32 s1, s0, 0x2aaaaaab
	s_lshr_b32 s16, s1, 31
	s_ashr_i32 s1, s1, 2
	s_add_i32 s1, s1, s16
	s_lshl_b32 s16, s1, 3
	s_sub_i32 s17, 64, s16
	s_min_i32 s17, s17, 8
	s_abs_i32 s22, s17
	v_cvt_f32_u32_e32 v2, s22
	s_sub_i32 s24, 0, s22
	s_mul_i32 s1, s1, 24
	s_sub_i32 s0, s0, s1
	v_rcp_iflag_f32_e32 v2, v2
	s_abs_i32 s1, s0
	s_xor_b32 s23, s0, s17
	s_ashr_i32 s23, s23, 31
	v_mul_f32_e32 v2, 0x4f7ffffe, v2
	v_cvt_u32_f32_e32 v2, v2
	s_nop 0
	v_readfirstlane_b32 s25, v2
	s_mul_i32 s24, s24, s25
	s_mul_hi_u32 s24, s25, s24
	s_add_i32 s25, s25, s24
	s_mul_hi_u32 s24, s1, s25
	s_mul_i32 s25, s24, s22
	s_sub_i32 s1, s1, s25
	s_add_i32 s48, s24, 1
	s_sub_i32 s25, s1, s22
	s_cmp_ge_u32 s1, s22
	s_cselect_b32 s24, s48, s24
	s_cselect_b32 s1, s25, s1
	s_add_i32 s25, s24, 1
	s_cmp_ge_u32 s1, s22
	s_cselect_b32 s1, s25, s24
	s_xor_b32 s1, s1, s23
	s_sub_i32 s48, s1, s23
	s_mul_i32 s1, s48, s17
	s_sub_i32 s0, s0, s1
	s_add_i32 s51, s16, s0
	s_lshl_b32 s50, s51, 8
	s_add_i32 s49, s50, 0x100

; __global__ void __launch_bounds__(NTHR, 2) mk(Params p) {
;     ...
;             { pg8::Gemm g{XB, WinT + (size_t)l * SZ_WIN, T, INCP, DM, DM, DM}; pg8::OffsetOrder S; S.init(T, 256, F.G, (int)((blockIdx.x + 64) % F.G)); S.pn0 = 16;
;               EpiProj E{PROJ, p.in[2] + (size_t)l * 2 * DM}; pg8::gemm_phase<EpiProj, pg8::OffsetOrder, true>(F.lds, g, S, E); }
.LBB0_588:
	v_cvt_f32_u32_e32 v1, s59
	v_readlane_b32 s0, v253, 2
	v_readlane_b32 s1, v253, 3
	s_sub_i32 s1, 0, s59
	v_rcp_iflag_f32_e32 v1, v1
	s_add_i32 s0, s0, 0x80
	v_mov_b32_e32 v2, v0
	v_mul_f32_e32 v1, 0x4f7ffffe, v1
	v_cvt_u32_f32_e32 v1, v1
	v_readfirstlane_b32 s14, v2
	v_readfirstlane_b32 s2, v1
	s_mul_i32 s1, s1, s2
	s_mul_hi_u32 s1, s2, s1
	s_add_i32 s2, s2, s1
	s_mul_hi_u32 s1, s0, s2
	s_mul_i32 s1, s1, s59
	s_sub_i32 s0, s0, s1
	s_sub_i32 s1, s0, s59
	s_cmp_ge_u32 s0, s59
	s_cselect_b32 s0, s1, s0
	s_sub_i32 s1, s0, s59
	s_cmp_ge_u32 s0, s59
	s_cselect_b32 s21, s1, s0
	s_cmp_lt_i32 s21, 64
	s_cselect_b64 s[0:1], -1, 0
	s_cmp_gt_i32 s21, 63
	s_cbranch_scc1 .LBB0_594
	s_ashr_i32 s2, s21, 31
	s_lshr_b32 s2, s2, 29
	s_add_i32 s6, s21, s2
	s_and_b32 s2, s6, -8
	s_sub_i32 s4, s21, s2
	s_cmp_gt_i32 s4, -1
	s_cbranch_scc0 .LBB0_591
	s_lshl_b32 s5, s4, 3
	s_ashr_i32 s2, s6, 3
	s_cbranch_execz .LBB0_592
	s_branch .LBB0_593

;     __device__ bool next(int i, Unit& u) const { const bool ok = StaticOrder::next(i, u); u.pn += pn0; return ok; }
;     __device__ bool next(int i, Unit& u) const {
;         const long L = (long)i * G + c; if (L >= nwg) return false;
;         int wgid = (int)L; { const int q = nwg / NXCD, r = nwg % NXCD, xcd = wgid % NXCD, off = wgid / NXCD; wgid = (xcd < r ? xcd * (q + 1) : r * (q + 1) + (xcd - r) * q) + off; }
;         const int nig = WGM * nN, gid = wgid / nig, fm = gid * WGM, gsz = (nM - fm) < WGM ? (nM - fm) : WGM;
;         u.pm = fm + ((wgid % nig) % gsz); u.pn = (wgid % nig) / gsz; u.e = 0; u.r0 = u.pm * BM; u.rend = u.r0 + BM; return true;
; __global__ void __launch_bounds__(NTHR, 2) mk(Params p) {
;     ...
;             { const int G3 = F.G - F.G / 4;
;               pg8::Gemm g{CKVN, WukvT + (size_t)l * SZ_WUKV, T, 1024, KVL, KVL, KVL}; pg8::StaticOrder S; S.init(T, 1024, G3, (int)blockIdx.x < G3 ? (int)blockIdx.x : (1 << 28));
;               EpiKV E{KB, VB}; pg8::gemm_phase<EpiKV, pg8::StaticOrder, true>(F.lds, g, S, E); }
.LBB0_2887:
	s_or_b64 exec, exec, s[2:3]
	s_lshr_b32 s0, s36, 30
	s_add_i32 s0, s59, s0
	s_ashr_i32 s0, s0, 2
	s_sub_i32 s33, s59, s0
	v_readlane_b32 s0, v253, 2
	s_add_i32 s37, s0, -64
	s_cmpk_lt_i32 s0, 0xc0
	s_cselect_b32 s37, 0x10000000, s37
	s_cmpk_lt_i32 s0, 0x80
	s_cselect_b32 s37, s0, s37
	v_readlane_b32 s1, v253, 3
	v_mov_b32_e32 v2, v0
	s_cmpk_lt_i32 s37, 0x100
	s_barrier
	s_cselect_b64 s[0:1], -1, 0
	s_cmpk_gt_i32 s37, 0xff
	v_readfirstlane_b32 s4, v2
	s_cbranch_scc1 .LBB0_2893
	s_ashr_i32 s2, s37, 31
	s_lshr_b32 s2, s2, 29
	s_add_i32 s7, s37, s2
	s_and_b32 s2, s7, -8
	s_sub_i32 s5, s37, s2
	s_cmp_gt_i32 s5, -1
	s_cbranch_scc0 .LBB0_2890
	s_lshl_b32 s6, s5, 5
	s_ashr_i32 s2, s7, 3
	s_cbranch_execz .LBB0_2891
	s_branch .LBB0_2892

;     __device__ bool next(int i, Unit& u) const { const bool ok = StaticOrder::next(i, u); u.pn += pn0; return ok; }
;     __device__ bool next(int i, Unit& u) const {
;         const long L = (long)i * G + c; if (L >= nwg) return false;
;         int wgid = (int)L; { const int q = nwg / NXCD, r = nwg % NXCD, xcd = wgid % NXCD, off = wgid / NXCD; wgid = (xcd < r ? xcd * (q + 1) : r * (q + 1) + (xcd - r) * q) + off; }
;         const int nig = WGM * nN, gid = wgid / nig, fm = gid * WGM, gsz = (nM - fm) < WGM ? (nM - fm) : WGM;
;         u.pm = fm + ((wgid % nig) % gsz); u.pn = (wgid % nig) / gsz; u.e = 0; u.r0 = u.pm * BM; u.rend = u.r0 + BM; return true;
.Lq19_1_1:
	s_mov_b32 s6, s2
	s_ashr_i32 s2, s2, 31
	s_lshr_b32 s2, s2, 29
	v_readlane_b32 s3, v253, 3
	s_add_i32 s2, s6, s2
	s_ashr_i32 s3, s2, 3
	s_and_b32 s2, s2, -8
	s_sub_i32 s2, s6, s2
	s_cmp_lt_i32 s2, 0
	s_cselect_b32 s5, 25, 24
	s_mul_i32 s2, s2, s5
	s_add_i32 s2, s2, s3
	s_mul_hi_i32 s3, s2, 0x2aaaaaab
	s_lshr_b32 s5, s3, 31
	s_ashr_i32 s3, s3, 2
	s_add_i32 s3, s3, s5
	s_lshl_b32 s5, s3, 3
	s_mul_i32 s3, s3, 24
	s_sub_i32 s2, s2, s3
	s_bfe_i32 s3, s2, 0x80000
	s_bfe_u32 s3, s3, 0x3000c
	s_add_i32 s3, s2, s3
	s_bfe_i32 s6, s3, 0x80000
	s_and_b32 s3, s3, 0xf8
	s_sub_i32 s2, s2, s3
	s_sext_i32_i8 s2, s2
	s_add_i32 s51, s5, s2
	s_sext_i32_i16 s6, s6
	s_lshl_b32 s18, s51, 8
	s_ashr_i32 s50, s6, 3
	s_add_i32 s19, s18, 0x100

;     __device__ __forceinline__ const char* b_ptr(const Gemm& g, const Unit& u) const { return (const char*)g.Bt + (size_t)u.pn * BM * g.ldb * 2; }
;     __device__ bool next(int i, Unit& u) const { const bool ok = StaticOrder::next(i, u); u.pn += pn0; return ok; }
; #define PG8_STAGE_B(bufoff, gbase) do { _Pragma("unroll") for (int _i = 0; _i < 2; ++_i) \
;         __builtin_amdgcn_global_load_lds((const unsigned*)((const char*)(gbase) + voffB[_i]), (LAS unsigned*)(lds + (bufoff) + ldsw + _i * 8192), 16, 0, 0); } while (0)
; #define PG8_STAGE_A(bufoff, V0, V1, kb) do { \
;         __builtin_amdgcn_global_load_lds((const unsigned*)((Abase + (kb)) + (V0)), (LAS unsigned*)(lds + (bufoff) + ldsw), 16, 0, 0); \
;         __builtin_amdgcn_global_load_lds((const unsigned*)((Abase + (kb)) + (V1)), (LAS unsigned*)(lds + (bufoff) + ldsw + 8192), 16, 0, 0); } while (0)
; #define PG8_WAIT_V(n) asm volatile("s_waitcnt vmcnt(" #n ")" ::: "memory")
; #define PG8_BAR __builtin_amdgcn_s_barrier()
;     __device__ __forceinline__ const char* b_ptr(const pg8::Gemm& g, const pg8::Unit& u) const { return (const char*)g.Bt + (size_t)u.e * strideE + (size_t)u.pn * 256 * g.ldb * 2; }
; template <class Epi, class Sched, bool ALIGN_EPI>
; __device__ __forceinline__ void gemm_phase(LAS unsigned char* lds, const Gemm g, const Sched& S, const Epi& E) {
;     ...
;     PG8_STAGE_B(PG8_SB(0, 0), cB); PG8_STAGE_B(PG8_SB(0, 1), cB + hstepB); PG8_STAGE_A(PG8_SA(0, 0), vc00, vc01, 0u); PG8_STAGE_A(PG8_SA(0, 1), vc10, vc11, 0u);
;     PG8_STAGE_B(PG8_SB(1, 0), cB + 128); PG8_STAGE_A(PG8_SA(1, 0), vc00, vc01, 128u); PG8_STAGE_B(PG8_SB(1, 1), cB + hstepB + 128);
;     if (wr == 1) PG8_BAR;
;     PG8_WAIT_V(8); PG8_BAR;
;     PG8_WAIT_V(6); PG8_BAR;
;     }
;     for (;;) {
;         const bool has_next = S.next(ui + 1, nxt);
;         const char* nB = cB; const float* pbn = pbc;
;         if constexpr (Sched::BF32) { if (has_next) pbn = S.bsrc(nxt, bh); } else { if (has_next) nB = S.b_ptr(g, nxt); }
;         unsigned vn00 = vc00, vn01 = vc01, vn10 = vc10, vn11 = vc11;
;         if (has_next) { PG8_VOFF(vn, nxt); }
.LBB0_2991:
	v_lshrrev_b32_e32 v5, 1, v2
	v_and_b32_e32 v5, 24, v5
	v_and_b32_e32 v4, 15, v2
	v_lshlrev_b32_e32 v6, 1, v5
	v_lshlrev_b32_e32 v2, 2, v2
	v_lshl_or_b32 v203, s0, 6, v4
	s_lshl_b32 s0, s0, 13
	v_lshl_or_b32 v4, v4, 6, v6
	v_and_b32_e32 v2, 32, v2
	v_bitop3_b32 v6, v4, s0, v2 bitop3:0xde
	s_lshl_b32 s0, s1, 5
	s_and_b32 s0, s0, 0x60
	s_lshl_b32 s1, s0, 7
	s_waitcnt vmcnt(8)
	s_barrier
	s_waitcnt vmcnt(6)
	s_cmpk_lt_u32 s4, 0x100
	v_readlane_b32 s4, v253, 2
	s_movk_i32 s38, 0x60
	v_bitop3_b32 v221, v4, s1, v2 bitop3:0xde
	s_cselect_b64 s[12:13], -1, 0
	s_bitcmp0_b32 s4, 7
	s_cbranch_scc1 .Lq19_1_2
	s_xor_b32 s4, s4, 64
.Lq19_1_2:
	s_ashr_i32 s39, s4, 31
	v_or_b32_e32 v223, s0, v5
	v_mov_b64_e32 v[206:207], 0xc0
	v_mov_b64_e32 v[208:209], 0xbf
	s_mov_b32 s40, 0x2aaaaaab
	s_add_i32 s41, 0, 0x10000
	s_add_i32 s42, 0, 0x14000
	s_add_i32 s43, 0, 0x18000
	s_add_i32 s44, 0, 0x1c000
	s_mov_b32 s14, 0x3e16c740
	s_movk_i32 s45, 0x600
	v_add_u32_e32 v234, 0, v6
	s_barrier
	v_readlane_b32 s5, v253, 3
	s_branch .LBB0_2994

;     __device__ bool next(int i, Unit& u) const { const bool ok = StaticOrder::next(i, u); u.pn += pn0; return ok; }
;     __device__ bool next(int i, Unit& u) const {
;         const long L = (long)i * G + c; if (L >= nwg) return false;
;         int wgid = (int)L; { const int q = nwg / NXCD, r = nwg % NXCD, xcd = wgid % NXCD, off = wgid / NXCD; wgid = (xcd < r ? xcd * (q + 1) : r * (q + 1) + (xcd - r) * q) + off; }
;         const int nig = WGM * nN, gid = wgid / nig, fm = gid * WGM, gsz = (nM - fm) < WGM ? (nM - fm) : WGM;
;         u.pm = fm + ((wgid % nig) % gsz); u.pn = (wgid % nig) / gsz; u.e = 0; u.r0 = u.pm * BM; u.rend = u.r0 + BM; return true;
; template <class Epi, class Sched, bool ALIGN_EPI>
; __device__ __forceinline__ void gemm_phase(LAS unsigned char* lds, const Gemm g, const Sched& S, const Epi& E) {
;     ...
;         const bool has_next = S.next(ui + 1, nxt);
.LBB0_2994:
	s_add_i32 s37, s37, 1
	s_mul_i32 s0, s37, s36
	s_mul_hi_u32 s1, s37, s59
	s_add_i32 s1, s1, s0
	s_mul_i32 s0, s37, s59
	v_readlane_b32 s4, v253, 2
	s_bitcmp0_b32 s4, 7
	s_cbranch_scc1 .Lq19_1_3
	s_xor_b32 s4, s4, 64
.Lq19_1_3:
	s_add_u32 s0, s0, s4
	s_addc_u32 s1, s1, s39
	v_readlane_b32 s5, v253, 3
	v_cmp_gt_i64_e32 vcc, s[0:1], v[208:209]
	v_cmp_lt_i64_e64 s[4:5], s[0:1], v[206:207]
	s_cbranch_vccnz .LBB0_2996
	s_ashr_i32 s1, s0, 31
	s_lshr_b32 s1, s1, 29
	s_add_i32 s1, s0, s1
	s_ashr_i32 s16, s1, 3
	s_and_b32 s1, s1, -8
	s_sub_i32 s0, s0, s1
	s_cmp_lt_i32 s0, 0
	s_cselect_b32 s1, 25, 24
	s_mul_i32 s0, s0, s1
	s_add_i32 s0, s0, s16
	s_mul_hi_i32 s1, s0, 0x2aaaaaab
	s_lshr_b32 s16, s1, 31
	s_ashr_i32 s1, s1, 2
	s_add_i32 s1, s1, s16
	s_lshl_b32 s16, s1, 3
	s_sub_i32 s17, 64, s16
	s_min_i32 s17, s17, 8
	s_abs_i32 s22, s17
	v_cvt_f32_u32_e32 v2, s22
	s_sub_i32 s24, 0, s22
	s_mul_i32 s1, s1, 24
	s_sub_i32 s0, s0, s1
	v_rcp_iflag_f32_e32 v2, v2
	s_abs_i32 s1, s0
	s_xor_b32 s23, s0, s17
	s_ashr_i32 s23, s23, 31
	v_mul_f32_e32 v2, 0x4f7ffffe, v2
	v_cvt_u32_f32_e32 v2, v2
	s_nop 0
	v_readfirstlane_b32 s25, v2
	s_mul_i32 s24, s24, s25
	s_mul_hi_u32 s24, s25, s24
	s_add_i32 s25, s25, s24
	s_mul_hi_u32 s24, s1, s25
	s_mul_i32 s25, s24, s22
	s_sub_i32 s1, s1, s25
	s_add_i32 s46, s24, 1
	s_sub_i32 s25, s1, s22
	s_cmp_ge_u32 s1, s22
	s_cselect_b32 s24, s46, s24
	s_cselect_b32 s1, s25, s1
	s_add_i32 s25, s24, 1
	s_cmp_ge_u32 s1, s22
	s_cselect_b32 s1, s25, s24
	s_xor_b32 s1, s1, s23
	s_sub_i32 s46, s1, s23
	s_mul_i32 s1, s46, s17
	s_sub_i32 s0, s0, s1
	s_add_i32 s49, s16, s0
	s_lshl_b32 s48, s49, 8
	s_add_i32 s47, s48, 0x100

; __global__ void __launch_bounds__(NTHR, 2) mk(Params p) {
;     ...
;             { pg8::Gemm g{XB, WinT + (size_t)l * SZ_WIN, T, INCP, DM, DM, DM}; pg8::OffsetOrder S; S.init(T, 256, F.G, (int)((blockIdx.x + 64) % F.G)); S.pn0 = 16;
;               EpiProj E{PROJ, p.in[2] + (size_t)l * 2 * DM}; pg8::gemm_phase<EpiProj, pg8::OffsetOrder, true>(F.lds, g, S, E); }
.LBB0_3047:
	v_cvt_f32_u32_e32 v1, s59
	v_readlane_b32 s0, v253, 2
	v_readlane_b32 s1, v253, 3
	s_sub_i32 s1, 0, s59
	v_rcp_iflag_f32_e32 v1, v1
	s_add_i32 s0, s0, 0x80
	v_mov_b32_e32 v2, v0
	v_mul_f32_e32 v1, 0x4f7ffffe, v1
	v_cvt_u32_f32_e32 v1, v1
	v_readfirstlane_b32 s6, v2
	v_readfirstlane_b32 s2, v1
	s_mul_i32 s1, s1, s2
	s_mul_hi_u32 s1, s2, s1
	s_add_i32 s2, s2, s1
	s_mul_hi_u32 s1, s0, s2
	s_mul_i32 s1, s1, s59
	s_sub_i32 s0, s0, s1
	s_sub_i32 s1, s0, s59
	s_cmp_ge_u32 s0, s59
	s_cselect_b32 s0, s1, s0
	s_sub_i32 s1, s0, s59
	s_cmp_ge_u32 s0, s59
	s_cselect_b32 s21, s1, s0
	s_cmp_lt_i32 s21, 64
	s_cselect_b64 s[0:1], -1, 0
	s_cmp_gt_i32 s21, 63
	s_cbranch_scc1 .LBB0_3053
	s_ashr_i32 s2, s21, 31
	s_lshr_b32 s2, s2, 29
	s_add_i32 s7, s21, s2
	s_and_b32 s2, s7, -8
	s_sub_i32 s4, s21, s2
	s_cmp_gt_i32 s4, -1
	s_cbranch_scc0 .LBB0_3050
	s_lshl_b32 s5, s4, 3
	s_ashr_i32 s2, s7, 3
	s_cbranch_execz .LBB0_3051
	s_branch .LBB0_3052
